# t23
# baseline (speedup 1.0000x reference)
_Z11align_fusedPKfS0_PKiPf:
	s_load_dwordx8 s[4:11], s[0:1], 0x0
	s_sub_u32 s2, 0x1fff, s2
	s_mul_i32 s12, s2, 0x5dc0
	v_and_b32_e32 v7, 63, v0
	v_readfirstlane_b32 s13, v0
	v_lshlrev_b32_e32 v1, 4, v7
	v_mul_u32_u24_e32 v3, 12, v7
	s_mul_i32 s18, s13, 96
	s_mul_i32 s3, s13, 6
	s_sub_u32 s3, 0x49c, s3
	v_cmp_gt_u32_e64 s[14:15], s3, v7
	v_add_u32_e32 v2, s18, v1
	v_add_u32_e32 v3, s18, v3
	v_add_u32_e32 v4, 0x600, v3
	s_add_u32 s12, s12, s18
	s_add_u32 s12, s12, 0x800
	s_waitcnt lgkmcnt(0)
	s_sub_u32 s44, s12, 0x800
	s_add_u32 s40, s4, s44
	s_addc_u32 s41, s5, 0
	s_add_u32 s42, s40, 0x1000
	s_addc_u32 s43, s41, 0
	s_add_u32 s4, s4, s12
	s_addc_u32 s5, s5, 0
	s_add_u32 s10, s10, s12
	s_addc_u32 s11, s11, 0
	s_cmp_lg_u32 s13, 0
	s_cbranch_scc1 .Lbulk_waves
	v_lshlrev_b32_e32 v5, 2, v7
	global_load_dword v5, v5, s[8:9]
	global_load_dwordx3 v[44:46], v3, s[6:7]
	s_mov_b32 m0, s18
	s_nop 0
	global_load_lds_dwordx4 v1, s[40:41] nt
	global_load_lds_dwordx4 v1, s[40:41] offset:1024 nt
	global_load_lds_dwordx4 v1, s[40:41] offset:2048 nt
	global_load_lds_dwordx4 v1, s[40:41] offset:3072 nt
	s_add_u32 m0, s18, 0x1000
	s_nop 0
	global_load_lds_dwordx4 v1, s[42:43] nt
	global_load_lds_dwordx4 v1, s[42:43] offset:1024 nt
	s_mov_b32 s20, 0
	s_mov_b32 s21, 0x10000
	s_mov_b32 s22, 0
	s_mov_b32 s23, 0x20000
	s_mov_b32 s24, 0
	s_mov_b32 s25, 0x40000
	s_mov_b32 s26, 0
	s_mov_b32 s27, 0x80000
	s_waitcnt vmcnt(6)
	v_mul_u32_u24_e32 v5, 12, v5
	v_add_f32_dpp v52, v44, v44 quad_perm:[1,0,3,2] row_mask:0xf bank_mask:0xf
	v_add_f32_dpp v53, v45, v45 quad_perm:[1,0,3,2] row_mask:0xf bank_mask:0xf
	v_add_f32_dpp v54, v46, v46 quad_perm:[1,0,3,2] row_mask:0xf bank_mask:0xf
	v_add_f32_dpp v52, v52, v52 quad_perm:[2,3,0,1] row_mask:0xf bank_mask:0xf
	v_add_f32_dpp v53, v53, v53 quad_perm:[2,3,0,1] row_mask:0xf bank_mask:0xf
	v_add_f32_dpp v54, v54, v54 quad_perm:[2,3,0,1] row_mask:0xf bank_mask:0xf
	v_add_f32_dpp v52, v52, v52 row_half_mirror row_mask:0xf bank_mask:0xf
	v_add_f32_dpp v53, v53, v53 row_half_mirror row_mask:0xf bank_mask:0xf
	v_add_f32_dpp v54, v54, v54 row_half_mirror row_mask:0xf bank_mask:0xf
	v_add_f32_dpp v52, v52, v52 row_mirror row_mask:0xf bank_mask:0xf
	v_add_f32_dpp v53, v53, v53 row_mirror row_mask:0xf bank_mask:0xf
	v_add_f32_dpp v54, v54, v54 row_mirror row_mask:0xf bank_mask:0xf
	v_add_f32_dpp v52, v52, v52 row_bcast:15 row_mask:0xa bank_mask:0xf
	v_add_f32_dpp v53, v53, v53 row_bcast:15 row_mask:0xa bank_mask:0xf
	v_add_f32_dpp v54, v54, v54 row_bcast:15 row_mask:0xa bank_mask:0xf
	v_add_f32_dpp v52, v52, v52 row_bcast:31 row_mask:0xc bank_mask:0xf
	v_add_f32_dpp v53, v53, v53 row_bcast:31 row_mask:0xc bank_mask:0xf
	v_add_f32_dpp v54, v54, v54 row_bcast:31 row_mask:0xc bank_mask:0xf
	v_readlane_b32 s28, v52, 63
	v_readlane_b32 s29, v53, 63
	v_readlane_b32 s30, v54, 63
	v_mov_b32_e32 v52, s28
	v_mov_b32_e32 v53, s29
	v_mov_b32_e32 v54, s30
	v_fmac_f32_e32 v44, 0xbc800000, v52
	v_fmac_f32_e32 v45, 0xbc800000, v53
	v_fmac_f32_e32 v46, 0xbc800000, v54
	s_waitcnt vmcnt(0)
	s_waitcnt lgkmcnt(0)
	s_barrier
	ds_read2_b32 v[8:9], v3 offset0:0 offset1:1
	ds_read_b32 v24, v3 offset:8
	ds_read2_b32 v[10:11], v3 offset0:192 offset1:193
	ds_read_b32 v25, v3 offset:776
	ds_read2_b32 v[12:13], v4 offset0:0 offset1:1
	ds_read_b32 v26, v4 offset:8
	ds_read_b32 v48, v5
	ds_read_b32 v49, v5 offset:4
	ds_read_b32 v50, v5 offset:8
	s_waitcnt lgkmcnt(0)
	v_add_f32_dpp v52, v48, v48 quad_perm:[1,0,3,2] row_mask:0xf bank_mask:0xf
	v_add_f32_dpp v53, v49, v49 quad_perm:[1,0,3,2] row_mask:0xf bank_mask:0xf
	v_add_f32_dpp v54, v50, v50 quad_perm:[1,0,3,2] row_mask:0xf bank_mask:0xf
	v_add_f32_dpp v52, v52, v52 quad_perm:[2,3,0,1] row_mask:0xf bank_mask:0xf
	v_add_f32_dpp v53, v53, v53 quad_perm:[2,3,0,1] row_mask:0xf bank_mask:0xf
	v_add_f32_dpp v54, v54, v54 quad_perm:[2,3,0,1] row_mask:0xf bank_mask:0xf
	v_add_f32_dpp v52, v52, v52 row_half_mirror row_mask:0xf bank_mask:0xf
	v_add_f32_dpp v53, v53, v53 row_half_mirror row_mask:0xf bank_mask:0xf
	v_add_f32_dpp v54, v54, v54 row_half_mirror row_mask:0xf bank_mask:0xf
	v_add_f32_dpp v52, v52, v52 row_mirror row_mask:0xf bank_mask:0xf
	v_add_f32_dpp v53, v53, v53 row_mirror row_mask:0xf bank_mask:0xf
	v_add_f32_dpp v54, v54, v54 row_mirror row_mask:0xf bank_mask:0xf
	v_add_f32_dpp v52, v52, v52 row_bcast:15 row_mask:0xa bank_mask:0xf
	v_add_f32_dpp v53, v53, v53 row_bcast:15 row_mask:0xa bank_mask:0xf
	v_add_f32_dpp v54, v54, v54 row_bcast:15 row_mask:0xa bank_mask:0xf
	v_add_f32_dpp v52, v52, v52 row_bcast:31 row_mask:0xc bank_mask:0xf
	v_add_f32_dpp v53, v53, v53 row_bcast:31 row_mask:0xc bank_mask:0xf
	v_add_f32_dpp v54, v54, v54 row_bcast:31 row_mask:0xc bank_mask:0xf
	v_readlane_b32 s32, v52, 63
	v_readlane_b32 s33, v53, 63
	v_readlane_b32 s34, v54, 63
	v_mov_b32_e32 v52, s32
	v_mov_b32_e32 v53, s33
	v_mov_b32_e32 v54, s34
	v_fmac_f32_e32 v48, 0xbc800000, v52
	v_fmac_f32_e32 v49, 0xbc800000, v53
	v_fmac_f32_e32 v50, 0xbc800000, v54
	v_mul_f32_e32 v52, v48, v44
	v_mul_f32_e32 v53, v48, v45
	v_mul_f32_e32 v54, v48, v46
	v_mul_f32_e32 v55, v49, v44
	v_mul_f32_e32 v56, v49, v45
	v_mul_f32_e32 v57, v49, v46
	v_mul_f32_e32 v58, v50, v44
	v_mul_f32_e32 v59, v50, v45
	v_mul_f32_e32 v60, v50, v46
	v_add_f32_dpp v52, v52, v52 quad_perm:[1,0,3,2] row_mask:0xf bank_mask:0xf
	v_add_f32_dpp v53, v53, v53 quad_perm:[1,0,3,2] row_mask:0xf bank_mask:0xf
	v_add_f32_dpp v54, v54, v54 quad_perm:[1,0,3,2] row_mask:0xf bank_mask:0xf
	v_add_f32_dpp v55, v55, v55 quad_perm:[1,0,3,2] row_mask:0xf bank_mask:0xf
	v_add_f32_dpp v56, v56, v56 quad_perm:[1,0,3,2] row_mask:0xf bank_mask:0xf
	v_add_f32_dpp v57, v57, v57 quad_perm:[1,0,3,2] row_mask:0xf bank_mask:0xf
	v_add_f32_dpp v58, v58, v58 quad_perm:[1,0,3,2] row_mask:0xf bank_mask:0xf
	v_add_f32_dpp v59, v59, v59 quad_perm:[1,0,3,2] row_mask:0xf bank_mask:0xf
	v_add_f32_dpp v60, v60, v60 quad_perm:[1,0,3,2] row_mask:0xf bank_mask:0xf
	v_add_f32_dpp v52, v52, v52 quad_perm:[2,3,0,1] row_mask:0xf bank_mask:0xf
	v_add_f32_dpp v53, v53, v53 quad_perm:[2,3,0,1] row_mask:0xf bank_mask:0xf
	v_add_f32_dpp v54, v54, v54 quad_perm:[2,3,0,1] row_mask:0xf bank_mask:0xf
	v_add_f32_dpp v55, v55, v55 quad_perm:[2,3,0,1] row_mask:0xf bank_mask:0xf
	v_add_f32_dpp v56, v56, v56 quad_perm:[2,3,0,1] row_mask:0xf bank_mask:0xf
	v_add_f32_dpp v57, v57, v57 quad_perm:[2,3,0,1] row_mask:0xf bank_mask:0xf
	v_add_f32_dpp v58, v58, v58 quad_perm:[2,3,0,1] row_mask:0xf bank_mask:0xf
	v_add_f32_dpp v59, v59, v59 quad_perm:[2,3,0,1] row_mask:0xf bank_mask:0xf
	v_add_f32_dpp v60, v60, v60 quad_perm:[2,3,0,1] row_mask:0xf bank_mask:0xf
	v_add_f32_dpp v52, v52, v52 row_half_mirror row_mask:0xf bank_mask:0xf
	v_add_f32_dpp v53, v53, v53 row_half_mirror row_mask:0xf bank_mask:0xf
	v_add_f32_dpp v54, v54, v54 row_half_mirror row_mask:0xf bank_mask:0xf
	v_add_f32_dpp v55, v55, v55 row_half_mirror row_mask:0xf bank_mask:0xf
	v_add_f32_dpp v56, v56, v56 row_half_mirror row_mask:0xf bank_mask:0xf
	v_add_f32_dpp v57, v57, v57 row_half_mirror row_mask:0xf bank_mask:0xf
	v_add_f32_dpp v58, v58, v58 row_half_mirror row_mask:0xf bank_mask:0xf
	v_add_f32_dpp v59, v59, v59 row_half_mirror row_mask:0xf bank_mask:0xf
	v_add_f32_dpp v60, v60, v60 row_half_mirror row_mask:0xf bank_mask:0xf
	v_add_f32_dpp v52, v52, v52 row_mirror row_mask:0xf bank_mask:0xf
	v_add_f32_dpp v53, v53, v53 row_mirror row_mask:0xf bank_mask:0xf
	v_add_f32_dpp v54, v54, v54 row_mirror row_mask:0xf bank_mask:0xf
	v_add_f32_dpp v55, v55, v55 row_mirror row_mask:0xf bank_mask:0xf
	v_add_f32_dpp v56, v56, v56 row_mirror row_mask:0xf bank_mask:0xf
	v_add_f32_dpp v57, v57, v57 row_mirror row_mask:0xf bank_mask:0xf
	v_add_f32_dpp v58, v58, v58 row_mirror row_mask:0xf bank_mask:0xf
	v_add_f32_dpp v59, v59, v59 row_mirror row_mask:0xf bank_mask:0xf
	v_add_f32_dpp v60, v60, v60 row_mirror row_mask:0xf bank_mask:0xf
	v_add_f32_dpp v52, v52, v52 row_bcast:15 row_mask:0xa bank_mask:0xf
	v_add_f32_dpp v53, v53, v53 row_bcast:15 row_mask:0xa bank_mask:0xf
	v_add_f32_dpp v54, v54, v54 row_bcast:15 row_mask:0xa bank_mask:0xf
	v_add_f32_dpp v55, v55, v55 row_bcast:15 row_mask:0xa bank_mask:0xf
	v_add_f32_dpp v56, v56, v56 row_bcast:15 row_mask:0xa bank_mask:0xf
	v_add_f32_dpp v57, v57, v57 row_bcast:15 row_mask:0xa bank_mask:0xf
	v_add_f32_dpp v58, v58, v58 row_bcast:15 row_mask:0xa bank_mask:0xf
	v_add_f32_dpp v59, v59, v59 row_bcast:15 row_mask:0xa bank_mask:0xf
	v_add_f32_dpp v60, v60, v60 row_bcast:15 row_mask:0xa bank_mask:0xf
	v_add_f32_dpp v52, v52, v52 row_bcast:31 row_mask:0xc bank_mask:0xf
	v_add_f32_dpp v53, v53, v53 row_bcast:31 row_mask:0xc bank_mask:0xf
	v_add_f32_dpp v54, v54, v54 row_bcast:31 row_mask:0xc bank_mask:0xf
	v_add_f32_dpp v55, v55, v55 row_bcast:31 row_mask:0xc bank_mask:0xf
	v_add_f32_dpp v56, v56, v56 row_bcast:31 row_mask:0xc bank_mask:0xf
	v_add_f32_dpp v57, v57, v57 row_bcast:31 row_mask:0xc bank_mask:0xf
	v_add_f32_dpp v58, v58, v58 row_bcast:31 row_mask:0xc bank_mask:0xf
	v_add_f32_dpp v59, v59, v59 row_bcast:31 row_mask:0xc bank_mask:0xf
	v_add_f32_dpp v60, v60, v60 row_bcast:31 row_mask:0xc bank_mask:0xf
	v_cndmask_b32_e64 v52, v52, v55, s[22:23]
	v_cndmask_b32_e64 v53, v53, v56, s[22:23]
	v_cndmask_b32_e64 v54, v54, v57, s[22:23]
	v_cndmask_b32_e64 v52, v52, v58, s[24:25]
	v_cndmask_b32_e64 v53, v53, v59, s[24:25]
	v_cndmask_b32_e64 v54, v54, v60, s[24:25]
	v_cndmask_b32_e64 v52, v52, 0, s[26:27]
	v_cndmask_b32_e64 v53, v53, 0, s[26:27]
	v_cndmask_b32_e64 v54, v54, 0, s[26:27]
	v_cndmask_b32_e64 v40, 0, 1.0, s[20:21]
	v_cndmask_b32_e64 v41, 0, 1.0, s[22:23]
	v_cndmask_b32_e64 v42, 0, 1.0, s[24:25]
	v_mul_f32_e32 v55, v52, v52
	v_mul_f32_e32 v56, v53, v53
	v_mul_f32_e32 v57, v52, v53
	v_add_f32_dpp v55, v55, v55 quad_perm:[1,0,3,2] row_mask:0xf bank_mask:0xf
	v_add_f32_dpp v56, v56, v56 quad_perm:[1,0,3,2] row_mask:0xf bank_mask:0xf
	v_add_f32_dpp v57, v57, v57 quad_perm:[1,0,3,2] row_mask:0xf bank_mask:0xf
	v_add_f32_dpp v55, v55, v55 quad_perm:[2,3,0,1] row_mask:0xf bank_mask:0xf
	v_add_f32_dpp v56, v56, v56 quad_perm:[2,3,0,1] row_mask:0xf bank_mask:0xf
	v_add_f32_dpp v57, v57, v57 quad_perm:[2,3,0,1] row_mask:0xf bank_mask:0xf
	v_sub_f32_e32 v60, v56, v55
	v_mul_f32_e32 v58, v57, v57
	v_cmp_gt_f32_e32 vcc, 0, v60
	v_mul_f32_e32 v59, v60, v60
	v_fmac_f32_e32 v59, 4.0, v58
	v_sqrt_f32_e32 v59, v59
	s_nop 0
	v_add_f32_e64 v59, |v60|, v59
	v_add_f32_e32 v59, 0x0da24260, v59
	v_rcp_f32_e32 v59, v59
	v_add_f32_e32 v58, v57, v57
	v_mul_f32_e32 v59, v58, v59
	v_cndmask_b32_e64 v59, v59, -v59, vcc
	v_fma_f32 v58, v59, v59, 1.0
	v_rsq_f32_e32 v61, v58
	s_nop 0
	v_mul_f32_e32 v62, v61, v59
	v_mul_f32_e32 v55, v62, v53
	v_mul_f32_e32 v56, v62, v52
	v_fma_f32 v52, v61, v52, -v55
	v_fma_f32 v53, v61, v53, v56
	v_mul_f32_e32 v55, v52, v52
	v_mul_f32_e32 v56, v54, v54
	v_mul_f32_e32 v57, v52, v54
	v_add_f32_dpp v55, v55, v55 quad_perm:[1,0,3,2] row_mask:0xf bank_mask:0xf
	v_add_f32_dpp v56, v56, v56 quad_perm:[1,0,3,2] row_mask:0xf bank_mask:0xf
	v_add_f32_dpp v57, v57, v57 quad_perm:[1,0,3,2] row_mask:0xf bank_mask:0xf
	v_add_f32_dpp v55, v55, v55 quad_perm:[2,3,0,1] row_mask:0xf bank_mask:0xf
	v_add_f32_dpp v56, v56, v56 quad_perm:[2,3,0,1] row_mask:0xf bank_mask:0xf
	v_add_f32_dpp v57, v57, v57 quad_perm:[2,3,0,1] row_mask:0xf bank_mask:0xf
	v_sub_f32_e32 v60, v56, v55
	v_mul_f32_e32 v58, v57, v57
	v_cmp_gt_f32_e32 vcc, 0, v60
	v_mul_f32_e32 v59, v60, v60
	v_fmac_f32_e32 v59, 4.0, v58
	v_sqrt_f32_e32 v59, v59
	v_mul_f32_e32 v63, v62, v41
	v_mul_f32_e32 v43, v62, v40
	v_fma_f32 v40, v61, v40, -v63
	v_fma_f32 v41, v61, v41, v43
	v_add_f32_e64 v59, |v60|, v59
	v_add_f32_e32 v59, 0x0da24260, v59
	v_rcp_f32_e32 v59, v59
	v_add_f32_e32 v58, v57, v57
	v_mul_f32_e32 v59, v58, v59
	v_cndmask_b32_e64 v59, v59, -v59, vcc
	v_fma_f32 v58, v59, v59, 1.0
	v_rsq_f32_e32 v61, v58
	s_nop 0
	v_mul_f32_e32 v62, v61, v59
	v_mul_f32_e32 v55, v62, v54
	v_mul_f32_e32 v56, v62, v52
	v_fma_f32 v52, v61, v52, -v55
	v_fma_f32 v54, v61, v54, v56
	v_mul_f32_e32 v55, v53, v53
	v_mul_f32_e32 v56, v54, v54
	v_mul_f32_e32 v57, v53, v54
	v_add_f32_dpp v55, v55, v55 quad_perm:[1,0,3,2] row_mask:0xf bank_mask:0xf
	v_add_f32_dpp v56, v56, v56 quad_perm:[1,0,3,2] row_mask:0xf bank_mask:0xf
	v_add_f32_dpp v57, v57, v57 quad_perm:[1,0,3,2] row_mask:0xf bank_mask:0xf
	v_add_f32_dpp v55, v55, v55 quad_perm:[2,3,0,1] row_mask:0xf bank_mask:0xf
	v_add_f32_dpp v56, v56, v56 quad_perm:[2,3,0,1] row_mask:0xf bank_mask:0xf
	v_add_f32_dpp v57, v57, v57 quad_perm:[2,3,0,1] row_mask:0xf bank_mask:0xf
	v_sub_f32_e32 v60, v56, v55
	v_mul_f32_e32 v58, v57, v57
	v_cmp_gt_f32_e32 vcc, 0, v60
	v_mul_f32_e32 v59, v60, v60
	v_fmac_f32_e32 v59, 4.0, v58
	v_sqrt_f32_e32 v59, v59
	v_mul_f32_e32 v63, v62, v42
	v_mul_f32_e32 v43, v62, v40
	v_fma_f32 v40, v61, v40, -v63
	v_fma_f32 v42, v61, v42, v43
	v_add_f32_e64 v59, |v60|, v59
	v_add_f32_e32 v59, 0x0da24260, v59
	v_rcp_f32_e32 v59, v59
	v_add_f32_e32 v58, v57, v57
	v_mul_f32_e32 v59, v58, v59
	v_cndmask_b32_e64 v59, v59, -v59, vcc
	v_fma_f32 v58, v59, v59, 1.0
	v_rsq_f32_e32 v61, v58
	s_nop 0
	v_mul_f32_e32 v62, v61, v59
	v_mul_f32_e32 v55, v62, v54
	v_mul_f32_e32 v56, v62, v53
	v_fma_f32 v53, v61, v53, -v55
	v_fma_f32 v54, v61, v54, v56
	v_mul_f32_e32 v55, v52, v52
	v_mul_f32_e32 v56, v53, v53
	v_mul_f32_e32 v57, v52, v53
	v_add_f32_dpp v55, v55, v55 quad_perm:[1,0,3,2] row_mask:0xf bank_mask:0xf
	v_add_f32_dpp v56, v56, v56 quad_perm:[1,0,3,2] row_mask:0xf bank_mask:0xf
	v_add_f32_dpp v57, v57, v57 quad_perm:[1,0,3,2] row_mask:0xf bank_mask:0xf
	v_add_f32_dpp v55, v55, v55 quad_perm:[2,3,0,1] row_mask:0xf bank_mask:0xf
	v_add_f32_dpp v56, v56, v56 quad_perm:[2,3,0,1] row_mask:0xf bank_mask:0xf
	v_add_f32_dpp v57, v57, v57 quad_perm:[2,3,0,1] row_mask:0xf bank_mask:0xf
	v_sub_f32_e32 v60, v56, v55
	v_mul_f32_e32 v58, v57, v57
	v_cmp_gt_f32_e32 vcc, 0, v60
	v_mul_f32_e32 v59, v60, v60
	v_fmac_f32_e32 v59, 4.0, v58
	v_sqrt_f32_e32 v59, v59
	v_mul_f32_e32 v63, v62, v42
	v_mul_f32_e32 v43, v62, v41
	v_fma_f32 v41, v61, v41, -v63
	v_fma_f32 v42, v61, v42, v43
	v_add_f32_e64 v59, |v60|, v59
	v_add_f32_e32 v59, 0x0da24260, v59
	v_rcp_f32_e32 v59, v59
	v_add_f32_e32 v58, v57, v57
	v_mul_f32_e32 v59, v58, v59
	v_cndmask_b32_e64 v59, v59, -v59, vcc
	v_fma_f32 v58, v59, v59, 1.0
	v_rsq_f32_e32 v61, v58
	s_nop 0
	v_mul_f32_e32 v62, v61, v59
	v_mul_f32_e32 v55, v62, v53
	v_mul_f32_e32 v56, v62, v52
	v_fma_f32 v52, v61, v52, -v55
	v_fma_f32 v53, v61, v53, v56
	v_mul_f32_e32 v55, v52, v52
	v_mul_f32_e32 v56, v54, v54
	v_mul_f32_e32 v57, v52, v54
	v_add_f32_dpp v55, v55, v55 quad_perm:[1,0,3,2] row_mask:0xf bank_mask:0xf
	v_add_f32_dpp v56, v56, v56 quad_perm:[1,0,3,2] row_mask:0xf bank_mask:0xf
	v_add_f32_dpp v57, v57, v57 quad_perm:[1,0,3,2] row_mask:0xf bank_mask:0xf
	v_add_f32_dpp v55, v55, v55 quad_perm:[2,3,0,1] row_mask:0xf bank_mask:0xf
	v_add_f32_dpp v56, v56, v56 quad_perm:[2,3,0,1] row_mask:0xf bank_mask:0xf
	v_add_f32_dpp v57, v57, v57 quad_perm:[2,3,0,1] row_mask:0xf bank_mask:0xf
	v_sub_f32_e32 v60, v56, v55
	v_mul_f32_e32 v58, v57, v57
	v_cmp_gt_f32_e32 vcc, 0, v60
	v_mul_f32_e32 v59, v60, v60
	v_fmac_f32_e32 v59, 4.0, v58
	v_sqrt_f32_e32 v59, v59
	v_mul_f32_e32 v63, v62, v41
	v_mul_f32_e32 v43, v62, v40
	v_fma_f32 v40, v61, v40, -v63
	v_fma_f32 v41, v61, v41, v43
	v_add_f32_e64 v59, |v60|, v59
	v_add_f32_e32 v59, 0x0da24260, v59
	v_rcp_f32_e32 v59, v59
	v_add_f32_e32 v58, v57, v57
	v_mul_f32_e32 v59, v58, v59
	v_cndmask_b32_e64 v59, v59, -v59, vcc
	v_fma_f32 v58, v59, v59, 1.0
	v_rsq_f32_e32 v61, v58
	s_nop 0
	v_mul_f32_e32 v62, v61, v59
	v_mul_f32_e32 v55, v62, v54
	v_mul_f32_e32 v56, v62, v52
	v_fma_f32 v52, v61, v52, -v55
	v_fma_f32 v54, v61, v54, v56
	v_mul_f32_e32 v55, v53, v53
	v_mul_f32_e32 v56, v54, v54
	v_mul_f32_e32 v57, v53, v54
	v_add_f32_dpp v55, v55, v55 quad_perm:[1,0,3,2] row_mask:0xf bank_mask:0xf
	v_add_f32_dpp v56, v56, v56 quad_perm:[1,0,3,2] row_mask:0xf bank_mask:0xf
	v_add_f32_dpp v57, v57, v57 quad_perm:[1,0,3,2] row_mask:0xf bank_mask:0xf
	v_add_f32_dpp v55, v55, v55 quad_perm:[2,3,0,1] row_mask:0xf bank_mask:0xf
	v_add_f32_dpp v56, v56, v56 quad_perm:[2,3,0,1] row_mask:0xf bank_mask:0xf
	v_add_f32_dpp v57, v57, v57 quad_perm:[2,3,0,1] row_mask:0xf bank_mask:0xf
	v_sub_f32_e32 v60, v56, v55
	v_mul_f32_e32 v58, v57, v57
	v_cmp_gt_f32_e32 vcc, 0, v60
	v_mul_f32_e32 v59, v60, v60
	v_fmac_f32_e32 v59, 4.0, v58
	v_sqrt_f32_e32 v59, v59
	v_mul_f32_e32 v63, v62, v42
	v_mul_f32_e32 v43, v62, v40
	v_fma_f32 v40, v61, v40, -v63
	v_fma_f32 v42, v61, v42, v43
	v_add_f32_e64 v59, |v60|, v59
	v_add_f32_e32 v59, 0x0da24260, v59
	v_rcp_f32_e32 v59, v59
	v_add_f32_e32 v58, v57, v57
	v_mul_f32_e32 v59, v58, v59
	v_cndmask_b32_e64 v59, v59, -v59, vcc
	v_fma_f32 v58, v59, v59, 1.0
	v_rsq_f32_e32 v61, v58
	s_nop 0
	v_mul_f32_e32 v62, v61, v59
	v_mul_f32_e32 v55, v62, v54
	v_mul_f32_e32 v56, v62, v53
	v_fma_f32 v53, v61, v53, -v55
	v_fma_f32 v54, v61, v54, v56
	v_mul_f32_e32 v55, v52, v52
	v_mul_f32_e32 v56, v53, v53
	v_mul_f32_e32 v57, v52, v53
	v_add_f32_dpp v55, v55, v55 quad_perm:[1,0,3,2] row_mask:0xf bank_mask:0xf
	v_add_f32_dpp v56, v56, v56 quad_perm:[1,0,3,2] row_mask:0xf bank_mask:0xf
	v_add_f32_dpp v57, v57, v57 quad_perm:[1,0,3,2] row_mask:0xf bank_mask:0xf
	v_add_f32_dpp v55, v55, v55 quad_perm:[2,3,0,1] row_mask:0xf bank_mask:0xf
	v_add_f32_dpp v56, v56, v56 quad_perm:[2,3,0,1] row_mask:0xf bank_mask:0xf
	v_add_f32_dpp v57, v57, v57 quad_perm:[2,3,0,1] row_mask:0xf bank_mask:0xf
	v_sub_f32_e32 v60, v56, v55
	v_mul_f32_e32 v58, v57, v57
	v_cmp_gt_f32_e32 vcc, 0, v60
	v_mul_f32_e32 v59, v60, v60
	v_fmac_f32_e32 v59, 4.0, v58
	v_sqrt_f32_e32 v59, v59
	v_mul_f32_e32 v63, v62, v42
	v_mul_f32_e32 v43, v62, v41
	v_fma_f32 v41, v61, v41, -v63
	v_fma_f32 v42, v61, v42, v43
	v_add_f32_e64 v59, |v60|, v59
	v_add_f32_e32 v59, 0x0da24260, v59
	v_rcp_f32_e32 v59, v59
	v_add_f32_e32 v58, v57, v57
	v_mul_f32_e32 v59, v58, v59
	v_cndmask_b32_e64 v59, v59, -v59, vcc
	v_fma_f32 v58, v59, v59, 1.0
	v_rsq_f32_e32 v61, v58
	s_nop 0
	v_mul_f32_e32 v62, v61, v59
	v_mul_f32_e32 v55, v62, v53
	v_mul_f32_e32 v56, v62, v52
	v_fma_f32 v52, v61, v52, -v55
	v_fma_f32 v53, v61, v53, v56
	v_mul_f32_e32 v55, v52, v52
	v_mul_f32_e32 v56, v54, v54
	v_mul_f32_e32 v57, v52, v54
	v_add_f32_dpp v55, v55, v55 quad_perm:[1,0,3,2] row_mask:0xf bank_mask:0xf
	v_add_f32_dpp v56, v56, v56 quad_perm:[1,0,3,2] row_mask:0xf bank_mask:0xf
	v_add_f32_dpp v57, v57, v57 quad_perm:[1,0,3,2] row_mask:0xf bank_mask:0xf
	v_add_f32_dpp v55, v55, v55 quad_perm:[2,3,0,1] row_mask:0xf bank_mask:0xf
	v_add_f32_dpp v56, v56, v56 quad_perm:[2,3,0,1] row_mask:0xf bank_mask:0xf
	v_add_f32_dpp v57, v57, v57 quad_perm:[2,3,0,1] row_mask:0xf bank_mask:0xf
	v_sub_f32_e32 v60, v56, v55
	v_mul_f32_e32 v58, v57, v57
	v_cmp_gt_f32_e32 vcc, 0, v60
	v_mul_f32_e32 v59, v60, v60
	v_fmac_f32_e32 v59, 4.0, v58
	v_sqrt_f32_e32 v59, v59
	v_mul_f32_e32 v63, v62, v41
	v_mul_f32_e32 v43, v62, v40
	v_fma_f32 v40, v61, v40, -v63
	v_fma_f32 v41, v61, v41, v43
	v_add_f32_e64 v59, |v60|, v59
	v_add_f32_e32 v59, 0x0da24260, v59
	v_rcp_f32_e32 v59, v59
	v_add_f32_e32 v58, v57, v57
	v_mul_f32_e32 v59, v58, v59
	v_cndmask_b32_e64 v59, v59, -v59, vcc
	v_fma_f32 v58, v59, v59, 1.0
	v_rsq_f32_e32 v61, v58
	s_nop 0
	v_mul_f32_e32 v62, v61, v59
	v_mul_f32_e32 v55, v62, v54
	v_mul_f32_e32 v56, v62, v52
	v_fma_f32 v52, v61, v52, -v55
	v_fma_f32 v54, v61, v54, v56
	v_mul_f32_e32 v55, v53, v53
	v_mul_f32_e32 v56, v54, v54
	v_mul_f32_e32 v57, v53, v54
	v_add_f32_dpp v55, v55, v55 quad_perm:[1,0,3,2] row_mask:0xf bank_mask:0xf
	v_add_f32_dpp v56, v56, v56 quad_perm:[1,0,3,2] row_mask:0xf bank_mask:0xf
	v_add_f32_dpp v57, v57, v57 quad_perm:[1,0,3,2] row_mask:0xf bank_mask:0xf
	v_add_f32_dpp v55, v55, v55 quad_perm:[2,3,0,1] row_mask:0xf bank_mask:0xf
	v_add_f32_dpp v56, v56, v56 quad_perm:[2,3,0,1] row_mask:0xf bank_mask:0xf
	v_add_f32_dpp v57, v57, v57 quad_perm:[2,3,0,1] row_mask:0xf bank_mask:0xf
	v_sub_f32_e32 v60, v56, v55
	v_mul_f32_e32 v58, v57, v57
	v_cmp_gt_f32_e32 vcc, 0, v60
	v_mul_f32_e32 v59, v60, v60
	v_fmac_f32_e32 v59, 4.0, v58
	v_sqrt_f32_e32 v59, v59
	v_mul_f32_e32 v63, v62, v42
	v_mul_f32_e32 v43, v62, v40
	v_fma_f32 v40, v61, v40, -v63
	v_fma_f32 v42, v61, v42, v43
	v_add_f32_e64 v59, |v60|, v59
	v_add_f32_e32 v59, 0x0da24260, v59
	v_rcp_f32_e32 v59, v59
	v_add_f32_e32 v58, v57, v57
	v_mul_f32_e32 v59, v58, v59
	v_cndmask_b32_e64 v59, v59, -v59, vcc
	v_fma_f32 v58, v59, v59, 1.0
	v_rsq_f32_e32 v61, v58
	s_nop 0
	v_mul_f32_e32 v62, v61, v59
	v_mul_f32_e32 v55, v62, v54
	v_mul_f32_e32 v56, v62, v53
	v_fma_f32 v53, v61, v53, -v55
	v_fma_f32 v54, v61, v54, v56
	v_mul_f32_e32 v55, v52, v52
	v_mul_f32_e32 v56, v53, v53
	v_mul_f32_e32 v57, v52, v53
	v_add_f32_dpp v55, v55, v55 quad_perm:[1,0,3,2] row_mask:0xf bank_mask:0xf
	v_add_f32_dpp v56, v56, v56 quad_perm:[1,0,3,2] row_mask:0xf bank_mask:0xf
	v_add_f32_dpp v57, v57, v57 quad_perm:[1,0,3,2] row_mask:0xf bank_mask:0xf
	v_add_f32_dpp v55, v55, v55 quad_perm:[2,3,0,1] row_mask:0xf bank_mask:0xf
	v_add_f32_dpp v56, v56, v56 quad_perm:[2,3,0,1] row_mask:0xf bank_mask:0xf
	v_add_f32_dpp v57, v57, v57 quad_perm:[2,3,0,1] row_mask:0xf bank_mask:0xf
	v_sub_f32_e32 v60, v56, v55
	v_mul_f32_e32 v58, v57, v57
	v_cmp_gt_f32_e32 vcc, 0, v60
	v_mul_f32_e32 v59, v60, v60
	v_fmac_f32_e32 v59, 4.0, v58
	v_sqrt_f32_e32 v59, v59
	v_mul_f32_e32 v63, v62, v42
	v_mul_f32_e32 v43, v62, v41
	v_fma_f32 v41, v61, v41, -v63
	v_fma_f32 v42, v61, v42, v43
	v_add_f32_e64 v59, |v60|, v59
	v_add_f32_e32 v59, 0x0da24260, v59
	v_rcp_f32_e32 v59, v59
	v_add_f32_e32 v58, v57, v57
	v_mul_f32_e32 v59, v58, v59
	v_cndmask_b32_e64 v59, v59, -v59, vcc
	v_fma_f32 v58, v59, v59, 1.0
	v_rsq_f32_e32 v61, v58
	s_nop 0
	v_mul_f32_e32 v62, v61, v59
	v_mul_f32_e32 v55, v62, v53
	v_mul_f32_e32 v56, v62, v52
	v_fma_f32 v52, v61, v52, -v55
	v_fma_f32 v53, v61, v53, v56
	v_mul_f32_e32 v55, v52, v52
	v_mul_f32_e32 v56, v54, v54
	v_mul_f32_e32 v57, v52, v54
	v_add_f32_dpp v55, v55, v55 quad_perm:[1,0,3,2] row_mask:0xf bank_mask:0xf
	v_add_f32_dpp v56, v56, v56 quad_perm:[1,0,3,2] row_mask:0xf bank_mask:0xf
	v_add_f32_dpp v57, v57, v57 quad_perm:[1,0,3,2] row_mask:0xf bank_mask:0xf
	v_add_f32_dpp v55, v55, v55 quad_perm:[2,3,0,1] row_mask:0xf bank_mask:0xf
	v_add_f32_dpp v56, v56, v56 quad_perm:[2,3,0,1] row_mask:0xf bank_mask:0xf
	v_add_f32_dpp v57, v57, v57 quad_perm:[2,3,0,1] row_mask:0xf bank_mask:0xf
	v_sub_f32_e32 v60, v56, v55
	v_mul_f32_e32 v58, v57, v57
	v_cmp_gt_f32_e32 vcc, 0, v60
	v_mul_f32_e32 v59, v60, v60
	v_fmac_f32_e32 v59, 4.0, v58
	v_sqrt_f32_e32 v59, v59
	v_mul_f32_e32 v63, v62, v41
	v_mul_f32_e32 v43, v62, v40
	v_fma_f32 v40, v61, v40, -v63
	v_fma_f32 v41, v61, v41, v43
	v_add_f32_e64 v59, |v60|, v59
	v_add_f32_e32 v59, 0x0da24260, v59
	v_rcp_f32_e32 v59, v59
	v_add_f32_e32 v58, v57, v57
	v_mul_f32_e32 v59, v58, v59
	v_cndmask_b32_e64 v59, v59, -v59, vcc
	v_fma_f32 v58, v59, v59, 1.0
	v_rsq_f32_e32 v61, v58
	s_nop 0
	v_mul_f32_e32 v62, v61, v59
	v_mul_f32_e32 v55, v62, v54
	v_mul_f32_e32 v56, v62, v52
	v_fma_f32 v52, v61, v52, -v55
	v_fma_f32 v54, v61, v54, v56
	v_mul_f32_e32 v55, v53, v53
	v_mul_f32_e32 v56, v54, v54
	v_mul_f32_e32 v57, v53, v54
	v_add_f32_dpp v55, v55, v55 quad_perm:[1,0,3,2] row_mask:0xf bank_mask:0xf
	v_add_f32_dpp v56, v56, v56 quad_perm:[1,0,3,2] row_mask:0xf bank_mask:0xf
	v_add_f32_dpp v57, v57, v57 quad_perm:[1,0,3,2] row_mask:0xf bank_mask:0xf
	v_add_f32_dpp v55, v55, v55 quad_perm:[2,3,0,1] row_mask:0xf bank_mask:0xf
	v_add_f32_dpp v56, v56, v56 quad_perm:[2,3,0,1] row_mask:0xf bank_mask:0xf
	v_add_f32_dpp v57, v57, v57 quad_perm:[2,3,0,1] row_mask:0xf bank_mask:0xf
	v_sub_f32_e32 v60, v56, v55
	v_mul_f32_e32 v58, v57, v57
	v_cmp_gt_f32_e32 vcc, 0, v60
	v_mul_f32_e32 v59, v60, v60
	v_fmac_f32_e32 v59, 4.0, v58
	v_sqrt_f32_e32 v59, v59
	v_mul_f32_e32 v63, v62, v42
	v_mul_f32_e32 v43, v62, v40
	v_fma_f32 v40, v61, v40, -v63
	v_fma_f32 v42, v61, v42, v43
	v_add_f32_e64 v59, |v60|, v59
	v_add_f32_e32 v59, 0x0da24260, v59
	v_rcp_f32_e32 v59, v59
	v_add_f32_e32 v58, v57, v57
	v_mul_f32_e32 v59, v58, v59
	v_cndmask_b32_e64 v59, v59, -v59, vcc
	v_fma_f32 v58, v59, v59, 1.0
	v_rsq_f32_e32 v61, v58
	s_nop 0
	v_mul_f32_e32 v62, v61, v59
	v_mul_f32_e32 v55, v62, v54
	v_mul_f32_e32 v56, v62, v53
	v_fma_f32 v53, v61, v53, -v55
	v_fma_f32 v54, v61, v54, v56
	v_mul_f32_e32 v63, v62, v42
	v_mul_f32_e32 v43, v62, v41
	v_fma_f32 v41, v61, v41, -v63
	v_fma_f32 v42, v61, v42, v43
	v_mul_f32_e32 v55, v52, v52
	v_mul_f32_e32 v56, v53, v53
	v_mul_f32_e32 v57, v54, v54
	v_add_f32_dpp v55, v55, v55 quad_perm:[1,0,3,2] row_mask:0xf bank_mask:0xf
	v_add_f32_dpp v56, v56, v56 quad_perm:[1,0,3,2] row_mask:0xf bank_mask:0xf
	v_add_f32_dpp v57, v57, v57 quad_perm:[1,0,3,2] row_mask:0xf bank_mask:0xf
	v_add_f32_dpp v55, v55, v55 quad_perm:[2,3,0,1] row_mask:0xf bank_mask:0xf
	v_add_f32_dpp v56, v56, v56 quad_perm:[2,3,0,1] row_mask:0xf bank_mask:0xf
	v_add_f32_dpp v57, v57, v57 quad_perm:[2,3,0,1] row_mask:0xf bank_mask:0xf
	v_cmp_le_f32_e64 s[28:29], v55, v56
	v_cmp_le_f32_e64 s[30:31], v55, v57
	v_cmp_lt_f32_e32 vcc, v57, v56
	s_and_b64 s[28:29], s[28:29], s[30:31]
	s_andn2_b64 s[30:31], vcc, s[28:29]
	v_cndmask_b32_e64 v44, v52, v53, s[28:29]
	v_cndmask_b32_e64 v45, v54, v53, s[30:31]
	v_cndmask_b32_e64 v46, v40, v41, s[28:29]
	v_cndmask_b32_e64 v47, v42, v41, s[30:31]
	v_mul_f32_e32 v58, v44, v44
	s_nop 1
	v_add_f32_dpp v58, v58, v58 quad_perm:[1,0,3,2] row_mask:0xf bank_mask:0xf
	s_nop 1
	v_add_f32_dpp v58, v58, v58 quad_perm:[2,3,0,1] row_mask:0xf bank_mask:0xf
	v_max_f32_e32 v58, 0x3aa2425, v58
	v_rsq_f32_e32 v58, v58
	s_nop 0
	v_mul_f32_e32 v48, v44, v58
	v_mul_f32_e32 v59, v48, v45
	s_nop 1
	v_add_f32_dpp v59, v59, v59 quad_perm:[1,0,3,2] row_mask:0xf bank_mask:0xf
	s_nop 1
	v_add_f32_dpp v59, v59, v59 quad_perm:[2,3,0,1] row_mask:0xf bank_mask:0xf
	v_fma_f32 v49, -v59, v48, v45
	v_mul_f32_e32 v58, v49, v49
	s_nop 1
	v_add_f32_dpp v58, v58, v58 quad_perm:[1,0,3,2] row_mask:0xf bank_mask:0xf
	s_nop 1
	v_add_f32_dpp v58, v58, v58 quad_perm:[2,3,0,1] row_mask:0xf bank_mask:0xf
	v_max_f32_e32 v58, 0x3aa2425, v58
	v_rsq_f32_e32 v58, v58
	s_nop 0
	v_mul_f32_e32 v50, v49, v58
	v_mov_b32_dpp v43, v47 quad_perm:[2,0,1,3] row_mask:0xf bank_mask:0xf
	v_mov_b32_dpp v63, v47 quad_perm:[1,2,0,3] row_mask:0xf bank_mask:0xf
	v_mov_b32_dpp v62, v50 quad_perm:[2,0,1,3] row_mask:0xf bank_mask:0xf
	v_mov_b32_dpp v61, v50 quad_perm:[1,2,0,3] row_mask:0xf bank_mask:0xf
	v_mul_f32_dpp v60, v46, v43 quad_perm:[1,2,0,3] row_mask:0xf bank_mask:0xf
	v_mul_f32_dpp v51, v48, v62 quad_perm:[1,2,0,3] row_mask:0xf bank_mask:0xf
	s_nop 0
	v_fmac_f32_dpp v60, -v46, v63 quad_perm:[2,0,1,3] row_mask:0xf bank_mask:0xf
	v_fmac_f32_dpp v51, -v48, v61 quad_perm:[2,0,1,3] row_mask:0xf bank_mask:0xf
	v_mul_f32_dpp v52, v46, v48 quad_perm:[0,0,0,0] row_mask:0xf bank_mask:0xf
	v_mul_f32_dpp v53, v46, v48 quad_perm:[1,1,1,1] row_mask:0xf bank_mask:0xf
	v_mul_f32_dpp v54, v46, v48 quad_perm:[2,2,2,2] row_mask:0xf bank_mask:0xf
	v_fmac_f32_dpp v52, v47, v50 quad_perm:[0,0,0,0] row_mask:0xf bank_mask:0xf
	v_fmac_f32_dpp v53, v47, v50 quad_perm:[1,1,1,1] row_mask:0xf bank_mask:0xf
	v_fmac_f32_dpp v54, v47, v50 quad_perm:[2,2,2,2] row_mask:0xf bank_mask:0xf
	v_fmac_f32_dpp v52, v60, v51 quad_perm:[0,0,0,0] row_mask:0xf bank_mask:0xf
	v_fmac_f32_dpp v53, v60, v51 quad_perm:[1,1,1,1] row_mask:0xf bank_mask:0xf
	v_fmac_f32_dpp v54, v60, v51 quad_perm:[2,2,2,2] row_mask:0xf bank_mask:0xf
	v_mov_b32_e32 v55, 0
	v_writelane_b32 v55, s32, 48
	v_writelane_b32 v55, s33, 49
	v_writelane_b32 v55, s34, 50
	v_mul_f32_e32 v55, 0xbc800000, v55
	v_mul_f32_e32 v56, v55, v52
	v_mul_f32_e32 v57, v55, v53
	v_mul_f32_e32 v58, v55, v54
	v_add_f32_dpp v56, v56, v56 quad_perm:[1,0,3,2] row_mask:0xf bank_mask:0xf
	v_add_f32_dpp v57, v57, v57 quad_perm:[1,0,3,2] row_mask:0xf bank_mask:0xf
	v_add_f32_dpp v58, v58, v58 quad_perm:[1,0,3,2] row_mask:0xf bank_mask:0xf
	v_add_f32_dpp v56, v56, v56 quad_perm:[2,3,0,1] row_mask:0xf bank_mask:0xf
	v_add_f32_dpp v57, v57, v57 quad_perm:[2,3,0,1] row_mask:0xf bank_mask:0xf
	v_add_f32_dpp v58, v58, v58 quad_perm:[2,3,0,1] row_mask:0xf bank_mask:0xf
	v_cndmask_b32_e64 v52, v52, v56, s[26:27]
	v_cndmask_b32_e64 v53, v53, v57, s[26:27]
	v_cndmask_b32_e64 v54, v54, v58, s[26:27]
	v_subrev_u32_e32 v59, 48, v0
	v_lshlrev_b32_e32 v59, 4, v59
	s_mov_b32 s20, 0
	s_mov_b32 s21, 0xf0000
	s_mov_b64 exec, s[20:21]
	ds_write_b96 v59, v[52:54] offset:24576
	s_mov_b64 exec, -1
	s_waitcnt lgkmcnt(0)
	s_branch .Ljoin

.Ljoin:
	s_barrier
	v_mov_b32_e32 v6, 0x6000
	ds_read_b96 v[32:34], v6
	ds_read_b96 v[36:38], v6 offset:16
	ds_read_b96 v[40:42], v6 offset:32
	ds_read_b96 v[44:46], v6 offset:48
	v_add_u32_e32 v56, 0xc00, v3
	v_add_u32_e32 v57, 0x1200, v3
	s_waitcnt lgkmcnt(0)
	v_fma_f32 v60, v8, v32, v44
	v_fma_f32 v61, v8, v33, v45
	v_fma_f32 v62, v8, v34, v46
	v_fmac_f32_e32 v60, v9, v36
	v_fmac_f32_e32 v61, v9, v37
	v_fmac_f32_e32 v62, v9, v38
	v_fmac_f32_e32 v60, v24, v40
	v_fmac_f32_e32 v61, v24, v41
	v_fmac_f32_e32 v62, v24, v42
	ds_write2_b32 v3, v60, v61 offset0:0 offset1:1
	ds_write_b32 v3, v62 offset:8
	ds_read2_b32 v[14:15], v4 offset0:192 offset1:193
	ds_read_b32 v27, v4 offset:776
	v_fma_f32 v35, v10, v32, v44
	v_fma_f32 v39, v10, v33, v45
	v_fma_f32 v43, v10, v34, v46
	v_fmac_f32_e32 v35, v11, v36
	v_fmac_f32_e32 v39, v11, v37
	v_fmac_f32_e32 v43, v11, v38
	v_fmac_f32_e32 v35, v25, v40
	v_fmac_f32_e32 v39, v25, v41
	v_fmac_f32_e32 v43, v25, v42
	ds_write2_b32 v3, v35, v39 offset0:192 offset1:193
	ds_write_b32 v3, v43 offset:776
	ds_read2_b32 v[16:17], v56 offset0:0 offset1:1
	ds_read_b32 v28, v56 offset:8
	v_fma_f32 v60, v12, v32, v44
	v_fma_f32 v61, v12, v33, v45
	v_fma_f32 v62, v12, v34, v46
	v_fmac_f32_e32 v60, v13, v36
	v_fmac_f32_e32 v61, v13, v37
	v_fmac_f32_e32 v62, v13, v38
	v_fmac_f32_e32 v60, v26, v40
	v_fmac_f32_e32 v61, v26, v41
	v_fmac_f32_e32 v62, v26, v42
	ds_write2_b32 v4, v60, v61 offset0:0 offset1:1
	ds_write_b32 v4, v62 offset:8
	ds_read2_b32 v[18:19], v56 offset0:192 offset1:193
	ds_read_b32 v29, v56 offset:776
	s_waitcnt lgkmcnt(8)
	v_fma_f32 v35, v14, v32, v44
	v_fma_f32 v39, v14, v33, v45
	v_fma_f32 v43, v14, v34, v46
	v_fmac_f32_e32 v35, v15, v36
	v_fmac_f32_e32 v39, v15, v37
	v_fmac_f32_e32 v43, v15, v38
	v_fmac_f32_e32 v35, v27, v40
	v_fmac_f32_e32 v39, v27, v41
	v_fmac_f32_e32 v43, v27, v42
	ds_write2_b32 v4, v35, v39 offset0:192 offset1:193
	ds_write_b32 v4, v43 offset:776
	ds_read2_b32 v[20:21], v57 offset0:0 offset1:1
	ds_read_b32 v30, v57 offset:8
	s_waitcnt lgkmcnt(8)
	v_fma_f32 v60, v16, v32, v44
	v_fma_f32 v61, v16, v33, v45
	v_fma_f32 v62, v16, v34, v46
	v_fmac_f32_e32 v60, v17, v36
	v_fmac_f32_e32 v61, v17, v37
	v_fmac_f32_e32 v62, v17, v38
	v_fmac_f32_e32 v60, v28, v40
	v_fmac_f32_e32 v61, v28, v41
	v_fmac_f32_e32 v62, v28, v42
	ds_write2_b32 v56, v60, v61 offset0:0 offset1:1
	ds_write_b32 v56, v62 offset:8
	ds_read2_b32 v[22:23], v57 offset0:192 offset1:193
	ds_read_b32 v31, v57 offset:776
	s_waitcnt lgkmcnt(8)
	v_fma_f32 v35, v18, v32, v44
	v_fma_f32 v39, v18, v33, v45
	v_fma_f32 v43, v18, v34, v46
	v_fmac_f32_e32 v35, v19, v36
	v_fmac_f32_e32 v39, v19, v37
	v_fmac_f32_e32 v43, v19, v38
	v_fmac_f32_e32 v35, v29, v40
	v_fmac_f32_e32 v39, v29, v41
	v_fmac_f32_e32 v43, v29, v42
	ds_write2_b32 v56, v35, v39 offset0:192 offset1:193
	ds_write_b32 v56, v43 offset:776
	s_waitcnt lgkmcnt(6)
	v_fma_f32 v60, v20, v32, v44
	v_fma_f32 v61, v20, v33, v45
	v_fma_f32 v62, v20, v34, v46
	v_fmac_f32_e32 v60, v21, v36
	v_fmac_f32_e32 v61, v21, v37
	v_fmac_f32_e32 v62, v21, v38
	v_fmac_f32_e32 v60, v30, v40
	v_fmac_f32_e32 v61, v30, v41
	v_fmac_f32_e32 v62, v30, v42
	ds_write2_b32 v57, v60, v61 offset0:0 offset1:1
	ds_write_b32 v57, v62 offset:8
	s_waitcnt lgkmcnt(4)
	v_fma_f32 v35, v22, v32, v44
	v_fma_f32 v39, v22, v33, v45
	v_fma_f32 v43, v22, v34, v46
	v_fmac_f32_e32 v35, v23, v36
	v_fmac_f32_e32 v39, v23, v37
	v_fmac_f32_e32 v43, v23, v38
	v_fmac_f32_e32 v35, v31, v40
	v_fmac_f32_e32 v39, v31, v41
	v_fmac_f32_e32 v43, v31, v42
	ds_write2_b32 v57, v35, v39 offset0:192 offset1:193
	ds_write_b32 v57, v43 offset:776
	ds_read_b128 v[8:11], v2
	ds_read_b128 v[12:15], v2 offset:1024
	ds_read_b128 v[16:19], v2 offset:2048
	ds_read_b128 v[20:23], v2 offset:3072
	ds_read_b128 v[24:27], v2 offset:4096
	ds_read_b128 v[28:31], v2 offset:5120
	s_waitcnt lgkmcnt(5)
	global_store_dwordx4 v1, v[8:11], s[10:11] offset:-2048 sc1 nt
	s_waitcnt lgkmcnt(4)
	global_store_dwordx4 v1, v[12:15], s[10:11] offset:-1024 sc1 nt
	s_waitcnt lgkmcnt(3)
	global_store_dwordx4 v1, v[16:19], s[10:11] offset:0 sc1 nt
	s_waitcnt lgkmcnt(2)
	global_store_dwordx4 v1, v[20:23], s[10:11] offset:1024 sc1 nt
	s_waitcnt lgkmcnt(1)
	global_store_dwordx4 v1, v[24:27], s[10:11] offset:2048 sc1 nt
	s_waitcnt lgkmcnt(0)
	s_and_saveexec_b64 s[16:17], s[14:15]
	global_store_dwordx4 v1, v[28:31], s[10:11] offset:3072 sc1 nt
	s_endpgm
